# variant D plus gate/up next-unit gather offsets hoisted with exec-masked loads (valid rows only), one wait
# speedup vs baseline: 1.0028x; 1.0028x over previous
.LBB0_780:
	v_cndmask_b32_e64 v0, 0, 1, s[38:39]
	v_cmp_ne_u32_e64 s[2:3], 1, v0
	s_andn2_b64 vcc, exec, s[38:39]
	v_mov_b32_e32 v158, v140
	v_mov_b32_e32 v155, v134
	v_mov_b32_e32 v156, v136
	v_mov_b32_e32 v157, v138
	s_cbranch_vccnz .LBB0_790
	v_add_u32_e32 v200, s62, v146
	v_ashrrev_i32_e32 v201, 31, v200
	v_lshl_add_u64 v[200:201], v[200:201], 2, s[8:9]
	v_add_u32_e32 v202, s62, v147
	v_ashrrev_i32_e32 v203, 31, v202
	v_lshl_add_u64 v[202:203], v[202:203], 2, s[8:9]
	v_add_u32_e32 v204, s62, v148
	v_ashrrev_i32_e32 v205, 31, v204
	v_lshl_add_u64 v[204:205], v[204:205], 2, s[8:9]
	v_add_u32_e32 v206, s62, v149
	v_ashrrev_i32_e32 v207, 31, v206
	v_lshl_add_u64 v[206:207], v[206:207], 2, s[8:9]
	v_cmp_gt_i32_e32 vcc, s63, v146
	s_and_saveexec_b64 s[38:39], vcc
	global_load_dword v208, v[200:201], off
	s_or_b64 exec, exec, s[38:39]
	v_cmp_gt_i32_e32 vcc, s63, v147
	s_and_saveexec_b64 s[38:39], vcc
	global_load_dword v209, v[202:203], off
	s_or_b64 exec, exec, s[38:39]
	v_cmp_gt_i32_e32 vcc, s63, v148
	s_and_saveexec_b64 s[38:39], vcc
	global_load_dword v210, v[204:205], off
	s_or_b64 exec, exec, s[38:39]
	v_cmp_gt_i32_e32 vcc, s63, v149
	s_and_saveexec_b64 s[38:39], vcc
	global_load_dword v211, v[206:207], off
	s_or_b64 exec, exec, s[38:39]
	s_waitcnt vmcnt(0)
	v_lshlrev_b32_e32 v208, 10, v208
	v_lshlrev_b32_e32 v209, 10, v209
	v_lshlrev_b32_e32 v210, 10, v210
	v_lshlrev_b32_e32 v211, 10, v211
	v_and_b32_e32 v208, 0x3fff800, v208
	v_and_b32_e32 v209, 0x3fff800, v209
	v_and_b32_e32 v210, 0x3fff800, v210
	v_and_b32_e32 v211, 0x3fff800, v211
	v_cmp_gt_i32_e32 vcc, s63, v146
	s_nop 1
	v_cndmask_b32_e32 v0, 0, v208, vcc
	v_cmp_gt_i32_e32 vcc, s63, v147
	s_nop 1
	v_cndmask_b32_e32 v1, 0, v209, vcc
	v_cmp_gt_i32_e32 vcc, s63, v148
	s_nop 1
	v_cndmask_b32_e32 v3, 0, v210, vcc
	v_cmp_gt_i32_e32 vcc, s63, v149
	s_nop 1
	v_cndmask_b32_e32 v2, 0, v211, vcc

.LBB0_4344:
	v_cndmask_b32_e64 v0, 0, 1, s[38:39]
	v_cmp_ne_u32_e64 s[2:3], 1, v0
	s_andn2_b64 vcc, exec, s[38:39]
	v_mov_b32_e32 v158, v140
	v_mov_b32_e32 v155, v134
	v_mov_b32_e32 v156, v136
	v_mov_b32_e32 v157, v138
	s_cbranch_vccnz .LBB0_4354
	v_add_u32_e32 v200, s61, v146
	v_ashrrev_i32_e32 v201, 31, v200
	v_lshl_add_u64 v[200:201], v[200:201], 2, s[8:9]
	v_add_u32_e32 v202, s61, v147
	v_ashrrev_i32_e32 v203, 31, v202
	v_lshl_add_u64 v[202:203], v[202:203], 2, s[8:9]
	v_add_u32_e32 v204, s61, v148
	v_ashrrev_i32_e32 v205, 31, v204
	v_lshl_add_u64 v[204:205], v[204:205], 2, s[8:9]
	v_add_u32_e32 v206, s61, v149
	v_ashrrev_i32_e32 v207, 31, v206
	v_lshl_add_u64 v[206:207], v[206:207], 2, s[8:9]
	v_cmp_gt_i32_e32 vcc, s62, v146
	s_and_saveexec_b64 s[38:39], vcc
	global_load_dword v208, v[200:201], off
	s_or_b64 exec, exec, s[38:39]
	v_cmp_gt_i32_e32 vcc, s62, v147
	s_and_saveexec_b64 s[38:39], vcc
	global_load_dword v209, v[202:203], off
	s_or_b64 exec, exec, s[38:39]
	v_cmp_gt_i32_e32 vcc, s62, v148
	s_and_saveexec_b64 s[38:39], vcc
	global_load_dword v210, v[204:205], off
	s_or_b64 exec, exec, s[38:39]
	v_cmp_gt_i32_e32 vcc, s62, v149
	s_and_saveexec_b64 s[38:39], vcc
	global_load_dword v211, v[206:207], off
	s_or_b64 exec, exec, s[38:39]
	s_waitcnt vmcnt(0)
	v_lshlrev_b32_e32 v208, 10, v208
	v_lshlrev_b32_e32 v209, 10, v209
	v_lshlrev_b32_e32 v210, 10, v210
	v_lshlrev_b32_e32 v211, 10, v211
	v_and_b32_e32 v208, 0x3fff800, v208
	v_and_b32_e32 v209, 0x3fff800, v209
	v_and_b32_e32 v210, 0x3fff800, v210
	v_and_b32_e32 v211, 0x3fff800, v211
	v_cmp_gt_i32_e32 vcc, s62, v146
	s_nop 1
	v_cndmask_b32_e32 v0, 0, v208, vcc
	v_cmp_gt_i32_e32 vcc, s62, v147
	s_nop 1
	v_cndmask_b32_e32 v1, 0, v209, vcc
	v_cmp_gt_i32_e32 vcc, s62, v148
	s_nop 1
	v_cndmask_b32_e32 v3, 0, v210, vcc
	v_cmp_gt_i32_e32 vcc, s62, v149
	s_nop 1
	v_cndmask_b32_e32 v2, 0, v211, vcc
